# qkv: static s_setprio 2 for waves entering the temporal-attention epilogue
# speedup vs baseline: 1.0056x; 1.0003x over previous
_Z14k_qkv_temporalPKDF16_S0_PKfPDF16_S3_S3_PfPi:
	s_load_dwordx4 s[36:39], s[0:1], 0x0
	s_load_dwordx2 s[40:41], s[0:1], 0x10
	s_load_dwordx4 s[8:11], s[0:1], 0x30
	s_and_b32 s3, s2, 7
	s_mul_i32 s3, s3, 0x71
	s_lshr_b32 s4, s2, 3
	s_add_u32 s3, s3, s4
	s_and_b32 s22, s3, 7
	s_lshr_b32 s16, s3, 3
	s_mul_i32 s16, s16, 14
	v_lshrrev_b32_e32 v1, 6, v0
	v_and_b32_e32 v92, 15, v0
	v_bfe_u32 v90, v0, 4, 2
	v_lshlrev_b32_e32 v95, 2, v90
	v_lshl_or_b32 v91, v1, 5, v95
	v_bfe_u32 v162, v0, 3, 3
	v_and_b32_e32 v163, 7, v0
	v_lshrrev_b32_e32 v110, 1, v162
	v_and_b32_e32 v111, 1, v1
	v_lshl_or_b32 v110, v111, 2, v110
	v_xor_b32_e32 v110, v163, v110
	v_lshlrev_b32_e32 v110, 4, v110
	v_lshl_or_b32 v111, v1, 3, v162
	s_mov_b32 s42, 0x12492493
	s_movk_i32 s43, 0x627
	s_movk_i32 s44, 0x628
	v_add_u32_e32 v112, 0, v111
	v_min_u32_e32 v112, 0x7d, v112
	v_mul_hi_u32 v113, v112, s42
	v_mul_u32_u24_e32 v114, 14, v113
	v_sub_u32_e32 v114, v112, v114
	v_add_u32_e32 v114, s16, v114
	v_min_u32_e32 v114, s43, v114
	v_mad_u32_u24 v114, v113, s44, v114
	v_lshl_or_b32 v100, v114, 10, v110
	v_add_u32_e32 v112, 32, v111
	v_min_u32_e32 v112, 0x7d, v112
	v_mul_hi_u32 v113, v112, s42
	v_mul_u32_u24_e32 v114, 14, v113
	v_sub_u32_e32 v114, v112, v114
	v_add_u32_e32 v114, s16, v114
	v_min_u32_e32 v114, s43, v114
	v_mad_u32_u24 v114, v113, s44, v114
	v_lshl_or_b32 v101, v114, 10, v110
	v_add_u32_e32 v112, 64, v111
	v_min_u32_e32 v112, 0x7d, v112
	v_mul_hi_u32 v113, v112, s42
	v_mul_u32_u24_e32 v114, 14, v113
	v_sub_u32_e32 v114, v112, v114
	v_add_u32_e32 v114, s16, v114
	v_min_u32_e32 v114, s43, v114
	v_mad_u32_u24 v114, v113, s44, v114
	v_lshl_or_b32 v102, v114, 10, v110
	v_add_u32_e32 v112, 96, v111
	v_min_u32_e32 v112, 0x7d, v112
	v_mul_hi_u32 v113, v112, s42
	v_mul_u32_u24_e32 v114, 14, v113
	v_sub_u32_e32 v114, v112, v114
	v_add_u32_e32 v114, s16, v114
	v_min_u32_e32 v114, s43, v114
	v_mad_u32_u24 v114, v113, s44, v114
	v_lshl_or_b32 v103, v114, 10, v110
	s_lshl_b32 s45, s22, 6
	v_add_u32_e32 v112, s45, v111
	v_lshl_or_b32 v112, v112, 10, v110
	v_mov_b32_e32 v104, v112
	v_add_u32_e32 v105, 0x8000, v112
	v_add_u32_e32 v106, 0x80000, v112
	v_add_u32_e32 v107, 0x88000, v112
	v_add_u32_e32 v108, 0x100000, v112
	v_add_u32_e32 v109, 0x108000, v112
	v_lshlrev_b32_e32 v113, 10, v1
	s_nop 0
	v_readfirstlane_b32 s24, v113
	s_add_u32 s25, s24, 0x1000
	s_add_u32 s26, s24, 0x2000
	s_add_u32 s27, s24, 0x3000
	s_add_u32 s28, s24, 0x4000
	s_add_u32 s29, s24, 0x5000
	s_add_u32 s30, s24, 0x6000
	s_add_u32 s31, s24, 0x7000
	s_add_u32 s32, s24, 0x8000
	s_add_u32 s33, s24, 0x9000
	s_add_u32 s46, s24, 0xa000
	s_add_u32 s47, s25, 0xa000
	s_add_u32 s48, s26, 0xa000
	s_add_u32 s49, s27, 0xa000
	s_add_u32 s50, s28, 0xa000
	s_add_u32 s51, s29, 0xa000
	s_add_u32 s52, s30, 0xa000
	s_add_u32 s53, s31, 0xa000
	s_add_u32 s54, s32, 0xa000
	s_add_u32 s55, s33, 0xa000
	v_lshrrev_b32_e32 v113, 1, v92
	v_xor_b32_e32 v113, v90, v113
	v_lshlrev_b32_e32 v113, 4, v113
	v_lshl_or_b32 v160, v92, 7, v113
	v_xor_b32_e32 v161, 64, v160
	v_lshlrev_b32_e32 v114, 12, v1
	v_add_u32_e32 v158, v114, v160
	v_xor_b32_e32 v159, 64, v158
	v_lshl_add_u32 v114, s22, 6, v92
	v_lshlrev_b32_e32 v114, 2, v114
	v_add_u32_e32 v115, 0x1000, v114
	s_waitcnt lgkmcnt(0)
	global_load_dword v116, v114, s[40:41] offset:0
	global_load_dword v117, v114, s[40:41] offset:64
	global_load_dword v118, v114, s[40:41] offset:128
	global_load_dword v119, v114, s[40:41] offset:192
	global_load_dword v120, v114, s[40:41] offset:2048
	global_load_dword v121, v114, s[40:41] offset:2112
	global_load_dword v122, v114, s[40:41] offset:2176
	global_load_dword v123, v114, s[40:41] offset:2240
	global_load_dword v124, v115, s[40:41] offset:0
	global_load_dword v125, v115, s[40:41] offset:64
	global_load_dword v126, v115, s[40:41] offset:128
	global_load_dword v127, v115, s[40:41] offset:192
	s_mov_b32 m0, s24
	s_nop 0
	global_load_lds_dwordx4 v100, s[36:37]
	s_mov_b32 m0, s25
	s_nop 0
	global_load_lds_dwordx4 v101, s[36:37]
	s_mov_b32 m0, s26
	s_nop 0
	global_load_lds_dwordx4 v102, s[36:37]
	s_mov_b32 m0, s27
	s_nop 0
	global_load_lds_dwordx4 v103, s[36:37]
	s_mov_b32 m0, s28
	s_nop 0
	global_load_lds_dwordx4 v104, s[38:39]
	s_mov_b32 m0, s29
	s_nop 0
	global_load_lds_dwordx4 v105, s[38:39]
	s_mov_b32 m0, s30
	s_nop 0
	global_load_lds_dwordx4 v106, s[38:39]
	s_mov_b32 m0, s31
	s_nop 0
	global_load_lds_dwordx4 v107, s[38:39]
	s_mov_b32 m0, s32
	s_nop 0
	global_load_lds_dwordx4 v108, s[38:39]
	s_mov_b32 m0, s33
	s_nop 0
	global_load_lds_dwordx4 v109, s[38:39]
	s_add_u32 s36, s36, 0x80
	s_addc_u32 s37, s37, 0
	s_add_u32 s38, s38, 0x80
	s_addc_u32 s39, s39, 0
	s_waitcnt vmcnt(10)
	v_mov_b32_e32 v164, v116
	v_mov_b32_e32 v165, v116
	v_mov_b32_e32 v166, v116
	v_mov_b32_e32 v167, v116
	v_mov_b32_e32 v62, v116
	v_mov_b32_e32 v63, v116
	v_mov_b32_e32 v64, v116
	v_mov_b32_e32 v65, v116
	v_mov_b32_e32 v86, v117
	v_mov_b32_e32 v87, v117
	v_mov_b32_e32 v88, v117
	v_mov_b32_e32 v89, v117
	v_mov_b32_e32 v58, v117
	v_mov_b32_e32 v59, v117
	v_mov_b32_e32 v60, v117
	v_mov_b32_e32 v61, v117
	v_mov_b32_e32 v96, v118
	v_mov_b32_e32 v97, v118
	v_mov_b32_e32 v98, v118
	v_mov_b32_e32 v99, v118
	v_mov_b32_e32 v54, v118
	v_mov_b32_e32 v55, v118
	v_mov_b32_e32 v56, v118
	v_mov_b32_e32 v57, v118
	v_mov_b32_e32 v82, v119
	v_mov_b32_e32 v83, v119
	v_mov_b32_e32 v84, v119
	v_mov_b32_e32 v85, v119
	v_mov_b32_e32 v50, v119
	v_mov_b32_e32 v51, v119
	v_mov_b32_e32 v52, v119
	v_mov_b32_e32 v53, v119
	v_mov_b32_e32 v78, v120
	v_mov_b32_e32 v79, v120
	v_mov_b32_e32 v80, v120
	v_mov_b32_e32 v81, v120
	v_mov_b32_e32 v46, v120
	v_mov_b32_e32 v47, v120
	v_mov_b32_e32 v48, v120
	v_mov_b32_e32 v49, v120
	v_mov_b32_e32 v74, v121
	v_mov_b32_e32 v75, v121
	v_mov_b32_e32 v76, v121
	v_mov_b32_e32 v77, v121
	v_mov_b32_e32 v42, v121
	v_mov_b32_e32 v43, v121
	v_mov_b32_e32 v44, v121
	v_mov_b32_e32 v45, v121
	v_mov_b32_e32 v70, v122
	v_mov_b32_e32 v71, v122
	v_mov_b32_e32 v72, v122
	v_mov_b32_e32 v73, v122
	v_mov_b32_e32 v38, v122
	v_mov_b32_e32 v39, v122
	v_mov_b32_e32 v40, v122
	v_mov_b32_e32 v41, v122
	v_mov_b32_e32 v66, v123
	v_mov_b32_e32 v67, v123
	v_mov_b32_e32 v68, v123
	v_mov_b32_e32 v69, v123
	v_mov_b32_e32 v34, v123
	v_mov_b32_e32 v35, v123
	v_mov_b32_e32 v36, v123
	v_mov_b32_e32 v37, v123
	v_mov_b32_e32 v18, v124
	v_mov_b32_e32 v19, v124
	v_mov_b32_e32 v20, v124
	v_mov_b32_e32 v21, v124
	v_mov_b32_e32 v2, v124
	v_mov_b32_e32 v3, v124
	v_mov_b32_e32 v4, v124
	v_mov_b32_e32 v5, v124
	v_mov_b32_e32 v26, v125
	v_mov_b32_e32 v27, v125
	v_mov_b32_e32 v28, v125
	v_mov_b32_e32 v29, v125
	v_mov_b32_e32 v10, v125
	v_mov_b32_e32 v11, v125
	v_mov_b32_e32 v12, v125
	v_mov_b32_e32 v13, v125
	v_mov_b32_e32 v22, v126
	v_mov_b32_e32 v23, v126
	v_mov_b32_e32 v24, v126
	v_mov_b32_e32 v25, v126
	v_mov_b32_e32 v6, v126
	v_mov_b32_e32 v7, v126
	v_mov_b32_e32 v8, v126
	v_mov_b32_e32 v9, v126
	v_mov_b32_e32 v30, v127
	v_mov_b32_e32 v31, v127
	v_mov_b32_e32 v32, v127
	v_mov_b32_e32 v33, v127
	v_mov_b32_e32 v14, v127
	v_mov_b32_e32 v15, v127
	v_mov_b32_e32 v16, v127
	v_mov_b32_e32 v17, v127
	s_waitcnt vmcnt(0)
	s_barrier
	ds_read_b128 v[110:113], v158 offset:0
	ds_read_b128 v[114:117], v158 offset:2048
	ds_read_b128 v[118:121], v159 offset:0
	ds_read_b128 v[122:125], v159 offset:2048
	ds_read_b128 v[126:129], v160 offset:16384
	ds_read_b128 v[130:133], v160 offset:18432
	ds_read_b128 v[134:137], v160 offset:20480
	ds_read_b128 v[138:141], v160 offset:22528
	ds_read_b128 v[142:145], v160 offset:24576
	ds_read_b128 v[146:149], v160 offset:26624
	ds_read_b128 v[150:153], v160 offset:28672
	ds_read_b128 v[154:157], v160 offset:30720
	s_waitcnt lgkmcnt(7)
	v_mfma_f32_16x16x32_f16 v[164:167], v[110:113], v[126:129], v[164:167]
	v_mfma_f32_16x16x32_f16 v[62:65], v[114:117], v[126:129], v[62:65]
	ds_read_b128 v[126:129], v160 offset:32768
	s_waitcnt lgkmcnt(7)
	v_mfma_f32_16x16x32_f16 v[86:89], v[110:113], v[130:133], v[86:89]
	v_mfma_f32_16x16x32_f16 v[58:61], v[114:117], v[130:133], v[58:61]
	ds_read_b128 v[130:133], v160 offset:34816
	s_waitcnt lgkmcnt(10)
	s_barrier
	s_mov_b32 m0, s24
	s_nop 0
	global_load_lds_dwordx4 v100, s[36:37]
	s_mov_b32 m0, s25
	s_nop 0
	global_load_lds_dwordx4 v101, s[36:37]
	s_mov_b32 m0, s26
	s_nop 0
	global_load_lds_dwordx4 v102, s[36:37]
	s_mov_b32 m0, s27
	s_nop 0
	global_load_lds_dwordx4 v103, s[36:37]
	s_add_u32 s36, s36, 0x80
	s_addc_u32 s37, s37, 0
	s_waitcnt lgkmcnt(7)
	v_mfma_f32_16x16x32_f16 v[96:99], v[110:113], v[134:137], v[96:99]
	v_mfma_f32_16x16x32_f16 v[54:57], v[114:117], v[134:137], v[54:57]
	ds_read_b128 v[134:137], v160 offset:36864
	s_waitcnt lgkmcnt(7)
	v_mfma_f32_16x16x32_f16 v[82:85], v[110:113], v[138:141], v[82:85]
	v_mfma_f32_16x16x32_f16 v[50:53], v[114:117], v[138:141], v[50:53]
	ds_read_b128 v[138:141], v160 offset:38912
	s_waitcnt lgkmcnt(7)
	v_mfma_f32_16x16x32_f16 v[78:81], v[110:113], v[142:145], v[78:81]
	v_mfma_f32_16x16x32_f16 v[46:49], v[114:117], v[142:145], v[46:49]
	ds_read_b128 v[142:145], v161 offset:16384
	s_waitcnt lgkmcnt(7)
	v_mfma_f32_16x16x32_f16 v[74:77], v[110:113], v[146:149], v[74:77]
	v_mfma_f32_16x16x32_f16 v[42:45], v[114:117], v[146:149], v[42:45]
	ds_read_b128 v[146:149], v161 offset:18432
	s_waitcnt lgkmcnt(7)
	v_mfma_f32_16x16x32_f16 v[70:73], v[110:113], v[150:153], v[70:73]
	v_mfma_f32_16x16x32_f16 v[38:41], v[114:117], v[150:153], v[38:41]
	ds_read_b128 v[150:153], v161 offset:20480
	s_waitcnt lgkmcnt(7)
	v_mfma_f32_16x16x32_f16 v[66:69], v[110:113], v[154:157], v[66:69]
	v_mfma_f32_16x16x32_f16 v[34:37], v[114:117], v[154:157], v[34:37]
	ds_read_b128 v[154:157], v161 offset:22528
	s_waitcnt lgkmcnt(7)
	v_mfma_f32_16x16x32_f16 v[18:21], v[110:113], v[126:129], v[18:21]
	v_mfma_f32_16x16x32_f16 v[2:5], v[114:117], v[126:129], v[2:5]
	ds_read_b128 v[126:129], v161 offset:24576
	s_waitcnt lgkmcnt(7)
	v_mfma_f32_16x16x32_f16 v[26:29], v[110:113], v[130:133], v[26:29]
	v_mfma_f32_16x16x32_f16 v[10:13], v[114:117], v[130:133], v[10:13]
	ds_read_b128 v[130:133], v161 offset:26624
	s_waitcnt lgkmcnt(7)
	v_mfma_f32_16x16x32_f16 v[22:25], v[110:113], v[134:137], v[22:25]
	v_mfma_f32_16x16x32_f16 v[6:9], v[114:117], v[134:137], v[6:9]
	ds_read_b128 v[134:137], v161 offset:28672
	s_waitcnt lgkmcnt(7)
	v_mfma_f32_16x16x32_f16 v[30:33], v[110:113], v[138:141], v[30:33]
	v_mfma_f32_16x16x32_f16 v[14:17], v[114:117], v[138:141], v[14:17]
	ds_read_b128 v[138:141], v161 offset:30720
	s_waitcnt lgkmcnt(7)
	v_mfma_f32_16x16x32_f16 v[164:167], v[118:121], v[142:145], v[164:167]
	v_mfma_f32_16x16x32_f16 v[62:65], v[122:125], v[142:145], v[62:65]
	ds_read_b128 v[142:145], v161 offset:32768
	s_waitcnt lgkmcnt(7)
	v_mfma_f32_16x16x32_f16 v[86:89], v[118:121], v[146:149], v[86:89]
	v_mfma_f32_16x16x32_f16 v[58:61], v[122:125], v[146:149], v[58:61]
	ds_read_b128 v[146:149], v161 offset:34816
	s_waitcnt lgkmcnt(7)
	v_mfma_f32_16x16x32_f16 v[96:99], v[118:121], v[150:153], v[96:99]
	v_mfma_f32_16x16x32_f16 v[54:57], v[122:125], v[150:153], v[54:57]
	ds_read_b128 v[150:153], v161 offset:36864
	s_waitcnt lgkmcnt(7)
	v_mfma_f32_16x16x32_f16 v[82:85], v[118:121], v[154:157], v[82:85]
	v_mfma_f32_16x16x32_f16 v[50:53], v[122:125], v[154:157], v[50:53]
	ds_read_b128 v[154:157], v161 offset:38912
	s_waitcnt lgkmcnt(0)
	s_barrier
	s_mov_b32 m0, s28
	s_nop 0
	global_load_lds_dwordx4 v104, s[38:39]
	s_mov_b32 m0, s29
	s_nop 0
	global_load_lds_dwordx4 v105, s[38:39]
	s_mov_b32 m0, s30
	s_nop 0
	global_load_lds_dwordx4 v106, s[38:39]
	s_mov_b32 m0, s31
	s_nop 0
	global_load_lds_dwordx4 v107, s[38:39]
	s_mov_b32 m0, s32
	s_nop 0
	global_load_lds_dwordx4 v108, s[38:39]
	s_mov_b32 m0, s33
	s_nop 0
	global_load_lds_dwordx4 v109, s[38:39]
	s_add_u32 s38, s38, 0x80
	s_addc_u32 s39, s39, 0
	s_waitcnt lgkmcnt(7)
	v_mfma_f32_16x16x32_f16 v[78:81], v[118:121], v[126:129], v[78:81]
	v_mfma_f32_16x16x32_f16 v[46:49], v[122:125], v[126:129], v[46:49]
	s_waitcnt lgkmcnt(6)
	v_mfma_f32_16x16x32_f16 v[74:77], v[118:121], v[130:133], v[74:77]
	v_mfma_f32_16x16x32_f16 v[42:45], v[122:125], v[130:133], v[42:45]
	s_waitcnt lgkmcnt(5)
	v_mfma_f32_16x16x32_f16 v[70:73], v[118:121], v[134:137], v[70:73]
	v_mfma_f32_16x16x32_f16 v[38:41], v[122:125], v[134:137], v[38:41]
	s_waitcnt lgkmcnt(4)
	v_mfma_f32_16x16x32_f16 v[66:69], v[118:121], v[138:141], v[66:69]
	v_mfma_f32_16x16x32_f16 v[34:37], v[122:125], v[138:141], v[34:37]
	s_waitcnt lgkmcnt(3)
	v_mfma_f32_16x16x32_f16 v[18:21], v[118:121], v[142:145], v[18:21]
	v_mfma_f32_16x16x32_f16 v[2:5], v[122:125], v[142:145], v[2:5]
	s_waitcnt lgkmcnt(2)
	v_mfma_f32_16x16x32_f16 v[26:29], v[118:121], v[146:149], v[26:29]
	v_mfma_f32_16x16x32_f16 v[10:13], v[122:125], v[146:149], v[10:13]
	s_waitcnt lgkmcnt(1)
	v_mfma_f32_16x16x32_f16 v[22:25], v[118:121], v[150:153], v[22:25]
	v_mfma_f32_16x16x32_f16 v[6:9], v[122:125], v[150:153], v[6:9]
	s_waitcnt lgkmcnt(0)
	v_mfma_f32_16x16x32_f16 v[30:33], v[118:121], v[154:157], v[30:33]
	v_mfma_f32_16x16x32_f16 v[14:17], v[122:125], v[154:157], v[14:17]
	s_waitcnt vmcnt(0)
	s_barrier
	ds_read_b128 v[110:113], v158 offset:0
	ds_read_b128 v[114:117], v158 offset:2048
	ds_read_b128 v[118:121], v159 offset:0
	ds_read_b128 v[122:125], v159 offset:2048
	ds_read_b128 v[126:129], v160 offset:16384
	ds_read_b128 v[130:133], v160 offset:18432
	ds_read_b128 v[134:137], v160 offset:20480
	ds_read_b128 v[138:141], v160 offset:22528
	ds_read_b128 v[142:145], v160 offset:24576
	ds_read_b128 v[146:149], v160 offset:26624
	ds_read_b128 v[150:153], v160 offset:28672
	ds_read_b128 v[154:157], v160 offset:30720
	s_waitcnt lgkmcnt(7)
	v_mfma_f32_16x16x32_f16 v[164:167], v[110:113], v[126:129], v[164:167]
	v_mfma_f32_16x16x32_f16 v[62:65], v[114:117], v[126:129], v[62:65]
	ds_read_b128 v[126:129], v160 offset:32768
	s_waitcnt lgkmcnt(7)
	v_mfma_f32_16x16x32_f16 v[86:89], v[110:113], v[130:133], v[86:89]
	v_mfma_f32_16x16x32_f16 v[58:61], v[114:117], v[130:133], v[58:61]
	ds_read_b128 v[130:133], v160 offset:34816
	s_waitcnt lgkmcnt(10)
	s_barrier
	s_mov_b32 m0, s24
	s_nop 0
	global_load_lds_dwordx4 v100, s[36:37]
	s_mov_b32 m0, s25
	s_nop 0
	global_load_lds_dwordx4 v101, s[36:37]
	s_mov_b32 m0, s26
	s_nop 0
	global_load_lds_dwordx4 v102, s[36:37]
	s_mov_b32 m0, s27
	s_nop 0
	global_load_lds_dwordx4 v103, s[36:37]
	s_add_u32 s36, s36, 0x80
	s_addc_u32 s37, s37, 0
	s_waitcnt lgkmcnt(7)
	v_mfma_f32_16x16x32_f16 v[96:99], v[110:113], v[134:137], v[96:99]
	v_mfma_f32_16x16x32_f16 v[54:57], v[114:117], v[134:137], v[54:57]
	ds_read_b128 v[134:137], v160 offset:36864
	s_waitcnt lgkmcnt(7)
	v_mfma_f32_16x16x32_f16 v[82:85], v[110:113], v[138:141], v[82:85]
	v_mfma_f32_16x16x32_f16 v[50:53], v[114:117], v[138:141], v[50:53]
	ds_read_b128 v[138:141], v160 offset:38912
	s_waitcnt lgkmcnt(7)
	v_mfma_f32_16x16x32_f16 v[78:81], v[110:113], v[142:145], v[78:81]
	v_mfma_f32_16x16x32_f16 v[46:49], v[114:117], v[142:145], v[46:49]
	ds_read_b128 v[142:145], v161 offset:16384
	s_waitcnt lgkmcnt(7)
	v_mfma_f32_16x16x32_f16 v[74:77], v[110:113], v[146:149], v[74:77]
	v_mfma_f32_16x16x32_f16 v[42:45], v[114:117], v[146:149], v[42:45]
	ds_read_b128 v[146:149], v161 offset:18432
	s_waitcnt lgkmcnt(7)
	v_mfma_f32_16x16x32_f16 v[70:73], v[110:113], v[150:153], v[70:73]
	v_mfma_f32_16x16x32_f16 v[38:41], v[114:117], v[150:153], v[38:41]
	ds_read_b128 v[150:153], v161 offset:20480
	s_waitcnt lgkmcnt(7)
	v_mfma_f32_16x16x32_f16 v[66:69], v[110:113], v[154:157], v[66:69]
	v_mfma_f32_16x16x32_f16 v[34:37], v[114:117], v[154:157], v[34:37]
	ds_read_b128 v[154:157], v161 offset:22528
	s_waitcnt lgkmcnt(7)
	v_mfma_f32_16x16x32_f16 v[18:21], v[110:113], v[126:129], v[18:21]
	v_mfma_f32_16x16x32_f16 v[2:5], v[114:117], v[126:129], v[2:5]
	ds_read_b128 v[126:129], v161 offset:24576
	s_waitcnt lgkmcnt(7)
	v_mfma_f32_16x16x32_f16 v[26:29], v[110:113], v[130:133], v[26:29]
	v_mfma_f32_16x16x32_f16 v[10:13], v[114:117], v[130:133], v[10:13]
	ds_read_b128 v[130:133], v161 offset:26624
	s_waitcnt lgkmcnt(7)
	v_mfma_f32_16x16x32_f16 v[22:25], v[110:113], v[134:137], v[22:25]
	v_mfma_f32_16x16x32_f16 v[6:9], v[114:117], v[134:137], v[6:9]
	ds_read_b128 v[134:137], v161 offset:28672
	s_waitcnt lgkmcnt(7)
	v_mfma_f32_16x16x32_f16 v[30:33], v[110:113], v[138:141], v[30:33]
	v_mfma_f32_16x16x32_f16 v[14:17], v[114:117], v[138:141], v[14:17]
	ds_read_b128 v[138:141], v161 offset:30720
	s_waitcnt lgkmcnt(7)
	v_mfma_f32_16x16x32_f16 v[164:167], v[118:121], v[142:145], v[164:167]
	v_mfma_f32_16x16x32_f16 v[62:65], v[122:125], v[142:145], v[62:65]
	ds_read_b128 v[142:145], v161 offset:32768
	s_waitcnt lgkmcnt(7)
	v_mfma_f32_16x16x32_f16 v[86:89], v[118:121], v[146:149], v[86:89]
	v_mfma_f32_16x16x32_f16 v[58:61], v[122:125], v[146:149], v[58:61]
	ds_read_b128 v[146:149], v161 offset:34816
	s_waitcnt lgkmcnt(7)
	v_mfma_f32_16x16x32_f16 v[96:99], v[118:121], v[150:153], v[96:99]
	v_mfma_f32_16x16x32_f16 v[54:57], v[122:125], v[150:153], v[54:57]
	ds_read_b128 v[150:153], v161 offset:36864
	s_waitcnt lgkmcnt(7)
	v_mfma_f32_16x16x32_f16 v[82:85], v[118:121], v[154:157], v[82:85]
	v_mfma_f32_16x16x32_f16 v[50:53], v[122:125], v[154:157], v[50:53]
	ds_read_b128 v[154:157], v161 offset:38912
	s_waitcnt lgkmcnt(0)
	s_barrier
	s_mov_b32 m0, s28
	s_nop 0
	global_load_lds_dwordx4 v104, s[38:39]
	s_mov_b32 m0, s29
	s_nop 0
	global_load_lds_dwordx4 v105, s[38:39]
	s_mov_b32 m0, s30
	s_nop 0
	global_load_lds_dwordx4 v106, s[38:39]
	s_mov_b32 m0, s31
	s_nop 0
	global_load_lds_dwordx4 v107, s[38:39]
	s_mov_b32 m0, s32
	s_nop 0
	global_load_lds_dwordx4 v108, s[38:39]
	s_mov_b32 m0, s33
	s_nop 0
	global_load_lds_dwordx4 v109, s[38:39]
	s_add_u32 s38, s38, 0x80
	s_addc_u32 s39, s39, 0
	s_waitcnt lgkmcnt(7)
	v_mfma_f32_16x16x32_f16 v[78:81], v[118:121], v[126:129], v[78:81]
	v_mfma_f32_16x16x32_f16 v[46:49], v[122:125], v[126:129], v[46:49]
	s_waitcnt lgkmcnt(6)
	v_mfma_f32_16x16x32_f16 v[74:77], v[118:121], v[130:133], v[74:77]
	v_mfma_f32_16x16x32_f16 v[42:45], v[122:125], v[130:133], v[42:45]
	s_waitcnt lgkmcnt(5)
	v_mfma_f32_16x16x32_f16 v[70:73], v[118:121], v[134:137], v[70:73]
	v_mfma_f32_16x16x32_f16 v[38:41], v[122:125], v[134:137], v[38:41]
	s_waitcnt lgkmcnt(4)
	v_mfma_f32_16x16x32_f16 v[66:69], v[118:121], v[138:141], v[66:69]
	v_mfma_f32_16x16x32_f16 v[34:37], v[122:125], v[138:141], v[34:37]
	s_waitcnt lgkmcnt(3)
	v_mfma_f32_16x16x32_f16 v[18:21], v[118:121], v[142:145], v[18:21]
	v_mfma_f32_16x16x32_f16 v[2:5], v[122:125], v[142:145], v[2:5]
	s_waitcnt lgkmcnt(2)
	v_mfma_f32_16x16x32_f16 v[26:29], v[118:121], v[146:149], v[26:29]
	v_mfma_f32_16x16x32_f16 v[10:13], v[122:125], v[146:149], v[10:13]
	s_waitcnt lgkmcnt(1)
	v_mfma_f32_16x16x32_f16 v[22:25], v[118:121], v[150:153], v[22:25]
	v_mfma_f32_16x16x32_f16 v[6:9], v[122:125], v[150:153], v[6:9]
	s_waitcnt lgkmcnt(0)
	v_mfma_f32_16x16x32_f16 v[30:33], v[118:121], v[154:157], v[30:33]
	v_mfma_f32_16x16x32_f16 v[14:17], v[122:125], v[154:157], v[14:17]
	s_waitcnt vmcnt(0)
	s_barrier
	ds_read_b128 v[110:113], v158 offset:0
	ds_read_b128 v[114:117], v158 offset:2048
	ds_read_b128 v[118:121], v159 offset:0
	ds_read_b128 v[122:125], v159 offset:2048
	ds_read_b128 v[126:129], v160 offset:16384
	ds_read_b128 v[130:133], v160 offset:18432
	ds_read_b128 v[134:137], v160 offset:20480
	ds_read_b128 v[138:141], v160 offset:22528
	ds_read_b128 v[142:145], v160 offset:24576
	ds_read_b128 v[146:149], v160 offset:26624
	ds_read_b128 v[150:153], v160 offset:28672
	ds_read_b128 v[154:157], v160 offset:30720
	s_waitcnt lgkmcnt(7)
	v_mfma_f32_16x16x32_f16 v[164:167], v[110:113], v[126:129], v[164:167]
	v_mfma_f32_16x16x32_f16 v[62:65], v[114:117], v[126:129], v[62:65]
	ds_read_b128 v[126:129], v160 offset:32768
	s_waitcnt lgkmcnt(7)
	v_mfma_f32_16x16x32_f16 v[86:89], v[110:113], v[130:133], v[86:89]
	v_mfma_f32_16x16x32_f16 v[58:61], v[114:117], v[130:133], v[58:61]
	ds_read_b128 v[130:133], v160 offset:34816
	s_waitcnt lgkmcnt(10)
	s_barrier
	s_mov_b32 m0, s24
	s_nop 0
	global_load_lds_dwordx4 v100, s[36:37]
	s_mov_b32 m0, s25
	s_nop 0
	global_load_lds_dwordx4 v101, s[36:37]
	s_mov_b32 m0, s26
	s_nop 0
	global_load_lds_dwordx4 v102, s[36:37]
	s_mov_b32 m0, s27
	s_nop 0
	global_load_lds_dwordx4 v103, s[36:37]
	s_add_u32 s36, s36, 0x80
	s_addc_u32 s37, s37, 0
	s_waitcnt lgkmcnt(7)
	v_mfma_f32_16x16x32_f16 v[96:99], v[110:113], v[134:137], v[96:99]
	v_mfma_f32_16x16x32_f16 v[54:57], v[114:117], v[134:137], v[54:57]
	ds_read_b128 v[134:137], v160 offset:36864
	s_waitcnt lgkmcnt(7)
	v_mfma_f32_16x16x32_f16 v[82:85], v[110:113], v[138:141], v[82:85]
	v_mfma_f32_16x16x32_f16 v[50:53], v[114:117], v[138:141], v[50:53]
	ds_read_b128 v[138:141], v160 offset:38912
	s_waitcnt lgkmcnt(7)
	v_mfma_f32_16x16x32_f16 v[78:81], v[110:113], v[142:145], v[78:81]
	v_mfma_f32_16x16x32_f16 v[46:49], v[114:117], v[142:145], v[46:49]
	ds_read_b128 v[142:145], v161 offset:16384
	s_waitcnt lgkmcnt(7)
	v_mfma_f32_16x16x32_f16 v[74:77], v[110:113], v[146:149], v[74:77]
	v_mfma_f32_16x16x32_f16 v[42:45], v[114:117], v[146:149], v[42:45]
	ds_read_b128 v[146:149], v161 offset:18432
	s_waitcnt lgkmcnt(7)
	v_mfma_f32_16x16x32_f16 v[70:73], v[110:113], v[150:153], v[70:73]
	v_mfma_f32_16x16x32_f16 v[38:41], v[114:117], v[150:153], v[38:41]
	ds_read_b128 v[150:153], v161 offset:20480
	s_waitcnt lgkmcnt(7)
	v_mfma_f32_16x16x32_f16 v[66:69], v[110:113], v[154:157], v[66:69]
	v_mfma_f32_16x16x32_f16 v[34:37], v[114:117], v[154:157], v[34:37]
	ds_read_b128 v[154:157], v161 offset:22528
	s_waitcnt lgkmcnt(7)
	v_mfma_f32_16x16x32_f16 v[18:21], v[110:113], v[126:129], v[18:21]
	v_mfma_f32_16x16x32_f16 v[2:5], v[114:117], v[126:129], v[2:5]
	ds_read_b128 v[126:129], v161 offset:24576
	s_waitcnt lgkmcnt(7)
	v_mfma_f32_16x16x32_f16 v[26:29], v[110:113], v[130:133], v[26:29]
	v_mfma_f32_16x16x32_f16 v[10:13], v[114:117], v[130:133], v[10:13]
	ds_read_b128 v[130:133], v161 offset:26624
	s_waitcnt lgkmcnt(7)
	v_mfma_f32_16x16x32_f16 v[22:25], v[110:113], v[134:137], v[22:25]
	v_mfma_f32_16x16x32_f16 v[6:9], v[114:117], v[134:137], v[6:9]
	ds_read_b128 v[134:137], v161 offset:28672
	s_waitcnt lgkmcnt(7)
	v_mfma_f32_16x16x32_f16 v[30:33], v[110:113], v[138:141], v[30:33]
	v_mfma_f32_16x16x32_f16 v[14:17], v[114:117], v[138:141], v[14:17]
	ds_read_b128 v[138:141], v161 offset:30720
	s_waitcnt lgkmcnt(7)
	v_mfma_f32_16x16x32_f16 v[164:167], v[118:121], v[142:145], v[164:167]
	v_mfma_f32_16x16x32_f16 v[62:65], v[122:125], v[142:145], v[62:65]
	ds_read_b128 v[142:145], v161 offset:32768
	s_waitcnt lgkmcnt(7)
	v_mfma_f32_16x16x32_f16 v[86:89], v[118:121], v[146:149], v[86:89]
	v_mfma_f32_16x16x32_f16 v[58:61], v[122:125], v[146:149], v[58:61]
	ds_read_b128 v[146:149], v161 offset:34816
	s_waitcnt lgkmcnt(7)
	v_mfma_f32_16x16x32_f16 v[96:99], v[118:121], v[150:153], v[96:99]
	v_mfma_f32_16x16x32_f16 v[54:57], v[122:125], v[150:153], v[54:57]
	ds_read_b128 v[150:153], v161 offset:36864
	s_waitcnt lgkmcnt(7)
	v_mfma_f32_16x16x32_f16 v[82:85], v[118:121], v[154:157], v[82:85]
	v_mfma_f32_16x16x32_f16 v[50:53], v[122:125], v[154:157], v[50:53]
	ds_read_b128 v[154:157], v161 offset:38912
	s_waitcnt lgkmcnt(0)
	s_barrier
	s_mov_b32 m0, s28
	s_nop 0
	global_load_lds_dwordx4 v104, s[38:39]
	s_mov_b32 m0, s29
	s_nop 0
	global_load_lds_dwordx4 v105, s[38:39]
	s_mov_b32 m0, s30
	s_nop 0
	global_load_lds_dwordx4 v106, s[38:39]
	s_mov_b32 m0, s31
	s_nop 0
	global_load_lds_dwordx4 v107, s[38:39]
	s_mov_b32 m0, s32
	s_nop 0
	global_load_lds_dwordx4 v108, s[38:39]
	s_mov_b32 m0, s33
	s_nop 0
	global_load_lds_dwordx4 v109, s[38:39]
	s_add_u32 s38, s38, 0x80
	s_addc_u32 s39, s39, 0
	s_waitcnt lgkmcnt(7)
	v_mfma_f32_16x16x32_f16 v[78:81], v[118:121], v[126:129], v[78:81]
	v_mfma_f32_16x16x32_f16 v[46:49], v[122:125], v[126:129], v[46:49]
	s_waitcnt lgkmcnt(6)
	v_mfma_f32_16x16x32_f16 v[74:77], v[118:121], v[130:133], v[74:77]
	v_mfma_f32_16x16x32_f16 v[42:45], v[122:125], v[130:133], v[42:45]
	s_waitcnt lgkmcnt(5)
	v_mfma_f32_16x16x32_f16 v[70:73], v[118:121], v[134:137], v[70:73]
	v_mfma_f32_16x16x32_f16 v[38:41], v[122:125], v[134:137], v[38:41]
	s_waitcnt lgkmcnt(4)
	v_mfma_f32_16x16x32_f16 v[66:69], v[118:121], v[138:141], v[66:69]
	v_mfma_f32_16x16x32_f16 v[34:37], v[122:125], v[138:141], v[34:37]
	s_waitcnt lgkmcnt(3)
	v_mfma_f32_16x16x32_f16 v[18:21], v[118:121], v[142:145], v[18:21]
	v_mfma_f32_16x16x32_f16 v[2:5], v[122:125], v[142:145], v[2:5]
	s_waitcnt lgkmcnt(2)
	v_mfma_f32_16x16x32_f16 v[26:29], v[118:121], v[146:149], v[26:29]
	v_mfma_f32_16x16x32_f16 v[10:13], v[122:125], v[146:149], v[10:13]
	s_waitcnt lgkmcnt(1)
	v_mfma_f32_16x16x32_f16 v[22:25], v[118:121], v[150:153], v[22:25]
	v_mfma_f32_16x16x32_f16 v[6:9], v[122:125], v[150:153], v[6:9]
	s_waitcnt lgkmcnt(0)
	v_mfma_f32_16x16x32_f16 v[30:33], v[118:121], v[154:157], v[30:33]
	v_mfma_f32_16x16x32_f16 v[14:17], v[122:125], v[154:157], v[14:17]
	s_waitcnt vmcnt(0)
	s_barrier
	ds_read_b128 v[110:113], v158 offset:0
	ds_read_b128 v[114:117], v158 offset:2048
	ds_read_b128 v[118:121], v159 offset:0
	ds_read_b128 v[122:125], v159 offset:2048
	ds_read_b128 v[126:129], v160 offset:16384
	ds_read_b128 v[130:133], v160 offset:18432
	ds_read_b128 v[134:137], v160 offset:20480
	ds_read_b128 v[138:141], v160 offset:22528
	ds_read_b128 v[142:145], v160 offset:24576
	ds_read_b128 v[146:149], v160 offset:26624
	ds_read_b128 v[150:153], v160 offset:28672
	ds_read_b128 v[154:157], v160 offset:30720
	s_waitcnt lgkmcnt(7)
	v_mfma_f32_16x16x32_f16 v[164:167], v[110:113], v[126:129], v[164:167]
	v_mfma_f32_16x16x32_f16 v[62:65], v[114:117], v[126:129], v[62:65]
	ds_read_b128 v[126:129], v160 offset:32768
	s_waitcnt lgkmcnt(7)
	v_mfma_f32_16x16x32_f16 v[86:89], v[110:113], v[130:133], v[86:89]
	v_mfma_f32_16x16x32_f16 v[58:61], v[114:117], v[130:133], v[58:61]
	ds_read_b128 v[130:133], v160 offset:34816
	s_waitcnt lgkmcnt(10)
	s_barrier
	s_mov_b32 m0, s24
	s_nop 0
	global_load_lds_dwordx4 v100, s[36:37]
	s_mov_b32 m0, s25
	s_nop 0
	global_load_lds_dwordx4 v101, s[36:37]
	s_mov_b32 m0, s26
	s_nop 0
	global_load_lds_dwordx4 v102, s[36:37]
	s_mov_b32 m0, s27
	s_nop 0
	global_load_lds_dwordx4 v103, s[36:37]
	s_add_u32 s36, s36, 0x80
	s_addc_u32 s37, s37, 0
	s_waitcnt lgkmcnt(7)
	v_mfma_f32_16x16x32_f16 v[96:99], v[110:113], v[134:137], v[96:99]
	v_mfma_f32_16x16x32_f16 v[54:57], v[114:117], v[134:137], v[54:57]
	ds_read_b128 v[134:137], v160 offset:36864
	s_waitcnt lgkmcnt(7)
	v_mfma_f32_16x16x32_f16 v[82:85], v[110:113], v[138:141], v[82:85]
	v_mfma_f32_16x16x32_f16 v[50:53], v[114:117], v[138:141], v[50:53]
	ds_read_b128 v[138:141], v160 offset:38912
	s_waitcnt lgkmcnt(7)
	v_mfma_f32_16x16x32_f16 v[78:81], v[110:113], v[142:145], v[78:81]
	v_mfma_f32_16x16x32_f16 v[46:49], v[114:117], v[142:145], v[46:49]
	ds_read_b128 v[142:145], v161 offset:16384
	s_waitcnt lgkmcnt(7)
	v_mfma_f32_16x16x32_f16 v[74:77], v[110:113], v[146:149], v[74:77]
	v_mfma_f32_16x16x32_f16 v[42:45], v[114:117], v[146:149], v[42:45]
	ds_read_b128 v[146:149], v161 offset:18432
	s_waitcnt lgkmcnt(7)
	v_mfma_f32_16x16x32_f16 v[70:73], v[110:113], v[150:153], v[70:73]
	v_mfma_f32_16x16x32_f16 v[38:41], v[114:117], v[150:153], v[38:41]
	ds_read_b128 v[150:153], v161 offset:20480
	s_waitcnt lgkmcnt(7)
	v_mfma_f32_16x16x32_f16 v[66:69], v[110:113], v[154:157], v[66:69]
	v_mfma_f32_16x16x32_f16 v[34:37], v[114:117], v[154:157], v[34:37]
	ds_read_b128 v[154:157], v161 offset:22528
	s_waitcnt lgkmcnt(7)
	v_mfma_f32_16x16x32_f16 v[18:21], v[110:113], v[126:129], v[18:21]
	v_mfma_f32_16x16x32_f16 v[2:5], v[114:117], v[126:129], v[2:5]
	ds_read_b128 v[126:129], v161 offset:24576
	s_waitcnt lgkmcnt(7)
	v_mfma_f32_16x16x32_f16 v[26:29], v[110:113], v[130:133], v[26:29]
	v_mfma_f32_16x16x32_f16 v[10:13], v[114:117], v[130:133], v[10:13]
	ds_read_b128 v[130:133], v161 offset:26624
	s_waitcnt lgkmcnt(7)
	v_mfma_f32_16x16x32_f16 v[22:25], v[110:113], v[134:137], v[22:25]
	v_mfma_f32_16x16x32_f16 v[6:9], v[114:117], v[134:137], v[6:9]
	ds_read_b128 v[134:137], v161 offset:28672
	s_waitcnt lgkmcnt(7)
	v_mfma_f32_16x16x32_f16 v[30:33], v[110:113], v[138:141], v[30:33]
	v_mfma_f32_16x16x32_f16 v[14:17], v[114:117], v[138:141], v[14:17]
	ds_read_b128 v[138:141], v161 offset:30720
	s_waitcnt lgkmcnt(7)
	v_mfma_f32_16x16x32_f16 v[164:167], v[118:121], v[142:145], v[164:167]
	v_mfma_f32_16x16x32_f16 v[62:65], v[122:125], v[142:145], v[62:65]
	ds_read_b128 v[142:145], v161 offset:32768
	s_waitcnt lgkmcnt(7)
	v_mfma_f32_16x16x32_f16 v[86:89], v[118:121], v[146:149], v[86:89]
	v_mfma_f32_16x16x32_f16 v[58:61], v[122:125], v[146:149], v[58:61]
	ds_read_b128 v[146:149], v161 offset:34816
	s_waitcnt lgkmcnt(7)
	v_mfma_f32_16x16x32_f16 v[96:99], v[118:121], v[150:153], v[96:99]
	v_mfma_f32_16x16x32_f16 v[54:57], v[122:125], v[150:153], v[54:57]
	ds_read_b128 v[150:153], v161 offset:36864
	s_waitcnt lgkmcnt(7)
	v_mfma_f32_16x16x32_f16 v[82:85], v[118:121], v[154:157], v[82:85]
	v_mfma_f32_16x16x32_f16 v[50:53], v[122:125], v[154:157], v[50:53]
	ds_read_b128 v[154:157], v161 offset:38912
	s_waitcnt lgkmcnt(0)
	s_barrier
	s_mov_b32 m0, s28
	s_nop 0
	global_load_lds_dwordx4 v104, s[38:39]
	s_mov_b32 m0, s29
	s_nop 0
	global_load_lds_dwordx4 v105, s[38:39]
	s_mov_b32 m0, s30
	s_nop 0
	global_load_lds_dwordx4 v106, s[38:39]
	s_mov_b32 m0, s31
	s_nop 0
	global_load_lds_dwordx4 v107, s[38:39]
	s_mov_b32 m0, s32
	s_nop 0
	global_load_lds_dwordx4 v108, s[38:39]
	s_mov_b32 m0, s33
	s_nop 0
	global_load_lds_dwordx4 v109, s[38:39]
	s_add_u32 s38, s38, 0x80
	s_addc_u32 s39, s39, 0
	s_waitcnt lgkmcnt(7)
	v_mfma_f32_16x16x32_f16 v[78:81], v[118:121], v[126:129], v[78:81]
	v_mfma_f32_16x16x32_f16 v[46:49], v[122:125], v[126:129], v[46:49]
	s_waitcnt lgkmcnt(6)
	v_mfma_f32_16x16x32_f16 v[74:77], v[118:121], v[130:133], v[74:77]
	v_mfma_f32_16x16x32_f16 v[42:45], v[122:125], v[130:133], v[42:45]
	s_waitcnt lgkmcnt(5)
	v_mfma_f32_16x16x32_f16 v[70:73], v[118:121], v[134:137], v[70:73]
	v_mfma_f32_16x16x32_f16 v[38:41], v[122:125], v[134:137], v[38:41]
	s_waitcnt lgkmcnt(4)
	v_mfma_f32_16x16x32_f16 v[66:69], v[118:121], v[138:141], v[66:69]
	v_mfma_f32_16x16x32_f16 v[34:37], v[122:125], v[138:141], v[34:37]
	s_waitcnt lgkmcnt(3)
	v_mfma_f32_16x16x32_f16 v[18:21], v[118:121], v[142:145], v[18:21]
	v_mfma_f32_16x16x32_f16 v[2:5], v[122:125], v[142:145], v[2:5]
	s_waitcnt lgkmcnt(2)
	v_mfma_f32_16x16x32_f16 v[26:29], v[118:121], v[146:149], v[26:29]
	v_mfma_f32_16x16x32_f16 v[10:13], v[122:125], v[146:149], v[10:13]
	s_waitcnt lgkmcnt(1)
	v_mfma_f32_16x16x32_f16 v[22:25], v[118:121], v[150:153], v[22:25]
	v_mfma_f32_16x16x32_f16 v[6:9], v[122:125], v[150:153], v[6:9]
	s_waitcnt lgkmcnt(0)
	v_mfma_f32_16x16x32_f16 v[30:33], v[118:121], v[154:157], v[30:33]
	v_mfma_f32_16x16x32_f16 v[14:17], v[122:125], v[154:157], v[14:17]
	s_waitcnt vmcnt(0)
	s_barrier
	ds_read_b128 v[110:113], v158 offset:0
	ds_read_b128 v[114:117], v158 offset:2048
	ds_read_b128 v[118:121], v159 offset:0
	ds_read_b128 v[122:125], v159 offset:2048
	ds_read_b128 v[126:129], v160 offset:16384
	ds_read_b128 v[130:133], v160 offset:18432
	ds_read_b128 v[134:137], v160 offset:20480
	ds_read_b128 v[138:141], v160 offset:22528
	ds_read_b128 v[142:145], v160 offset:24576
	ds_read_b128 v[146:149], v160 offset:26624
	ds_read_b128 v[150:153], v160 offset:28672
	ds_read_b128 v[154:157], v160 offset:30720
	s_waitcnt lgkmcnt(7)
	v_mfma_f32_16x16x32_f16 v[164:167], v[110:113], v[126:129], v[164:167]
	v_mfma_f32_16x16x32_f16 v[62:65], v[114:117], v[126:129], v[62:65]
	ds_read_b128 v[126:129], v160 offset:32768
	s_waitcnt lgkmcnt(7)
	v_mfma_f32_16x16x32_f16 v[86:89], v[110:113], v[130:133], v[86:89]
	v_mfma_f32_16x16x32_f16 v[58:61], v[114:117], v[130:133], v[58:61]
	ds_read_b128 v[130:133], v160 offset:34816
	s_waitcnt lgkmcnt(10)
	s_barrier
	s_mov_b32 m0, s24
	s_nop 0
	global_load_lds_dwordx4 v100, s[36:37]
	s_mov_b32 m0, s25
	s_nop 0
	global_load_lds_dwordx4 v101, s[36:37]
	s_mov_b32 m0, s26
	s_nop 0
	global_load_lds_dwordx4 v102, s[36:37]
	s_mov_b32 m0, s27
	s_nop 0
	global_load_lds_dwordx4 v103, s[36:37]
	s_add_u32 s36, s36, 0x80
	s_addc_u32 s37, s37, 0
	s_waitcnt lgkmcnt(7)
	v_mfma_f32_16x16x32_f16 v[96:99], v[110:113], v[134:137], v[96:99]
	v_mfma_f32_16x16x32_f16 v[54:57], v[114:117], v[134:137], v[54:57]
	ds_read_b128 v[134:137], v160 offset:36864
	s_waitcnt lgkmcnt(7)
	v_mfma_f32_16x16x32_f16 v[82:85], v[110:113], v[138:141], v[82:85]
	v_mfma_f32_16x16x32_f16 v[50:53], v[114:117], v[138:141], v[50:53]
	ds_read_b128 v[138:141], v160 offset:38912
	s_waitcnt lgkmcnt(7)
	v_mfma_f32_16x16x32_f16 v[78:81], v[110:113], v[142:145], v[78:81]
	v_mfma_f32_16x16x32_f16 v[46:49], v[114:117], v[142:145], v[46:49]
	ds_read_b128 v[142:145], v161 offset:16384
	s_waitcnt lgkmcnt(7)
	v_mfma_f32_16x16x32_f16 v[74:77], v[110:113], v[146:149], v[74:77]
	v_mfma_f32_16x16x32_f16 v[42:45], v[114:117], v[146:149], v[42:45]
	ds_read_b128 v[146:149], v161 offset:18432
	s_waitcnt lgkmcnt(7)
	v_mfma_f32_16x16x32_f16 v[70:73], v[110:113], v[150:153], v[70:73]
	v_mfma_f32_16x16x32_f16 v[38:41], v[114:117], v[150:153], v[38:41]
	ds_read_b128 v[150:153], v161 offset:20480
	s_waitcnt lgkmcnt(7)
	v_mfma_f32_16x16x32_f16 v[66:69], v[110:113], v[154:157], v[66:69]
	v_mfma_f32_16x16x32_f16 v[34:37], v[114:117], v[154:157], v[34:37]
	ds_read_b128 v[154:157], v161 offset:22528
	s_waitcnt lgkmcnt(7)
	v_mfma_f32_16x16x32_f16 v[18:21], v[110:113], v[126:129], v[18:21]
	v_mfma_f32_16x16x32_f16 v[2:5], v[114:117], v[126:129], v[2:5]
	ds_read_b128 v[126:129], v161 offset:24576
	s_waitcnt lgkmcnt(7)
	v_mfma_f32_16x16x32_f16 v[26:29], v[110:113], v[130:133], v[26:29]
	v_mfma_f32_16x16x32_f16 v[10:13], v[114:117], v[130:133], v[10:13]
	ds_read_b128 v[130:133], v161 offset:26624
	s_waitcnt lgkmcnt(7)
	v_mfma_f32_16x16x32_f16 v[22:25], v[110:113], v[134:137], v[22:25]
	v_mfma_f32_16x16x32_f16 v[6:9], v[114:117], v[134:137], v[6:9]
	ds_read_b128 v[134:137], v161 offset:28672
	s_waitcnt lgkmcnt(7)
	v_mfma_f32_16x16x32_f16 v[30:33], v[110:113], v[138:141], v[30:33]
	v_mfma_f32_16x16x32_f16 v[14:17], v[114:117], v[138:141], v[14:17]
	ds_read_b128 v[138:141], v161 offset:30720
	s_waitcnt lgkmcnt(7)
	v_mfma_f32_16x16x32_f16 v[164:167], v[118:121], v[142:145], v[164:167]
	v_mfma_f32_16x16x32_f16 v[62:65], v[122:125], v[142:145], v[62:65]
	ds_read_b128 v[142:145], v161 offset:32768
	s_waitcnt lgkmcnt(7)
	v_mfma_f32_16x16x32_f16 v[86:89], v[118:121], v[146:149], v[86:89]
	v_mfma_f32_16x16x32_f16 v[58:61], v[122:125], v[146:149], v[58:61]
	ds_read_b128 v[146:149], v161 offset:34816
	s_waitcnt lgkmcnt(7)
	v_mfma_f32_16x16x32_f16 v[96:99], v[118:121], v[150:153], v[96:99]
	v_mfma_f32_16x16x32_f16 v[54:57], v[122:125], v[150:153], v[54:57]
	ds_read_b128 v[150:153], v161 offset:36864
	s_waitcnt lgkmcnt(7)
	v_mfma_f32_16x16x32_f16 v[82:85], v[118:121], v[154:157], v[82:85]
	v_mfma_f32_16x16x32_f16 v[50:53], v[122:125], v[154:157], v[50:53]
	ds_read_b128 v[154:157], v161 offset:38912
	s_waitcnt lgkmcnt(0)
	s_barrier
	s_mov_b32 m0, s28
	s_nop 0
	global_load_lds_dwordx4 v104, s[38:39]
	s_mov_b32 m0, s29
	s_nop 0
	global_load_lds_dwordx4 v105, s[38:39]
	s_mov_b32 m0, s30
	s_nop 0
	global_load_lds_dwordx4 v106, s[38:39]
	s_mov_b32 m0, s31
	s_nop 0
	global_load_lds_dwordx4 v107, s[38:39]
	s_mov_b32 m0, s32
	s_nop 0
	global_load_lds_dwordx4 v108, s[38:39]
	s_mov_b32 m0, s33
	s_nop 0
	global_load_lds_dwordx4 v109, s[38:39]
	s_add_u32 s38, s38, 0x80
	s_addc_u32 s39, s39, 0
	s_waitcnt lgkmcnt(7)
	v_mfma_f32_16x16x32_f16 v[78:81], v[118:121], v[126:129], v[78:81]
	v_mfma_f32_16x16x32_f16 v[46:49], v[122:125], v[126:129], v[46:49]
	s_waitcnt lgkmcnt(6)
	v_mfma_f32_16x16x32_f16 v[74:77], v[118:121], v[130:133], v[74:77]
	v_mfma_f32_16x16x32_f16 v[42:45], v[122:125], v[130:133], v[42:45]
	s_waitcnt lgkmcnt(5)
	v_mfma_f32_16x16x32_f16 v[70:73], v[118:121], v[134:137], v[70:73]
	v_mfma_f32_16x16x32_f16 v[38:41], v[122:125], v[134:137], v[38:41]
	s_waitcnt lgkmcnt(4)
	v_mfma_f32_16x16x32_f16 v[66:69], v[118:121], v[138:141], v[66:69]
	v_mfma_f32_16x16x32_f16 v[34:37], v[122:125], v[138:141], v[34:37]
	s_waitcnt lgkmcnt(3)
	v_mfma_f32_16x16x32_f16 v[18:21], v[118:121], v[142:145], v[18:21]
	v_mfma_f32_16x16x32_f16 v[2:5], v[122:125], v[142:145], v[2:5]
	s_waitcnt lgkmcnt(2)
	v_mfma_f32_16x16x32_f16 v[26:29], v[118:121], v[146:149], v[26:29]
	v_mfma_f32_16x16x32_f16 v[10:13], v[122:125], v[146:149], v[10:13]
	s_waitcnt lgkmcnt(1)
	v_mfma_f32_16x16x32_f16 v[22:25], v[118:121], v[150:153], v[22:25]
	v_mfma_f32_16x16x32_f16 v[6:9], v[122:125], v[150:153], v[6:9]
	s_waitcnt lgkmcnt(0)
	v_mfma_f32_16x16x32_f16 v[30:33], v[118:121], v[154:157], v[30:33]
	v_mfma_f32_16x16x32_f16 v[14:17], v[122:125], v[154:157], v[14:17]
	s_waitcnt vmcnt(0)
	s_barrier
	ds_read_b128 v[110:113], v158 offset:0
	ds_read_b128 v[114:117], v158 offset:2048
	ds_read_b128 v[118:121], v159 offset:0
	ds_read_b128 v[122:125], v159 offset:2048
	ds_read_b128 v[126:129], v160 offset:16384
	ds_read_b128 v[130:133], v160 offset:18432
	ds_read_b128 v[134:137], v160 offset:20480
	ds_read_b128 v[138:141], v160 offset:22528
	ds_read_b128 v[142:145], v160 offset:24576
	ds_read_b128 v[146:149], v160 offset:26624
	ds_read_b128 v[150:153], v160 offset:28672
	ds_read_b128 v[154:157], v160 offset:30720
	s_waitcnt lgkmcnt(7)
	v_mfma_f32_16x16x32_f16 v[164:167], v[110:113], v[126:129], v[164:167]
	v_mfma_f32_16x16x32_f16 v[62:65], v[114:117], v[126:129], v[62:65]
	ds_read_b128 v[126:129], v160 offset:32768
	s_waitcnt lgkmcnt(7)
	v_mfma_f32_16x16x32_f16 v[86:89], v[110:113], v[130:133], v[86:89]
	v_mfma_f32_16x16x32_f16 v[58:61], v[114:117], v[130:133], v[58:61]
	ds_read_b128 v[130:133], v160 offset:34816
	s_waitcnt lgkmcnt(10)
	s_barrier
	s_mov_b32 m0, s24
	s_nop 0
	global_load_lds_dwordx4 v100, s[36:37]
	s_mov_b32 m0, s25
	s_nop 0
	global_load_lds_dwordx4 v101, s[36:37]
	s_mov_b32 m0, s26
	s_nop 0
	global_load_lds_dwordx4 v102, s[36:37]
	s_mov_b32 m0, s27
	s_nop 0
	global_load_lds_dwordx4 v103, s[36:37]
	s_add_u32 s36, s36, 0x80
	s_addc_u32 s37, s37, 0
	s_waitcnt lgkmcnt(7)
	v_mfma_f32_16x16x32_f16 v[96:99], v[110:113], v[134:137], v[96:99]
	v_mfma_f32_16x16x32_f16 v[54:57], v[114:117], v[134:137], v[54:57]
	ds_read_b128 v[134:137], v160 offset:36864
	s_waitcnt lgkmcnt(7)
	v_mfma_f32_16x16x32_f16 v[82:85], v[110:113], v[138:141], v[82:85]
	v_mfma_f32_16x16x32_f16 v[50:53], v[114:117], v[138:141], v[50:53]
	ds_read_b128 v[138:141], v160 offset:38912
	s_waitcnt lgkmcnt(7)
	v_mfma_f32_16x16x32_f16 v[78:81], v[110:113], v[142:145], v[78:81]
	v_mfma_f32_16x16x32_f16 v[46:49], v[114:117], v[142:145], v[46:49]
	ds_read_b128 v[142:145], v161 offset:16384
	s_waitcnt lgkmcnt(7)
	v_mfma_f32_16x16x32_f16 v[74:77], v[110:113], v[146:149], v[74:77]
	v_mfma_f32_16x16x32_f16 v[42:45], v[114:117], v[146:149], v[42:45]
	ds_read_b128 v[146:149], v161 offset:18432
	s_waitcnt lgkmcnt(7)
	v_mfma_f32_16x16x32_f16 v[70:73], v[110:113], v[150:153], v[70:73]
	v_mfma_f32_16x16x32_f16 v[38:41], v[114:117], v[150:153], v[38:41]
	ds_read_b128 v[150:153], v161 offset:20480
	s_waitcnt lgkmcnt(7)
	v_mfma_f32_16x16x32_f16 v[66:69], v[110:113], v[154:157], v[66:69]
	v_mfma_f32_16x16x32_f16 v[34:37], v[114:117], v[154:157], v[34:37]
	ds_read_b128 v[154:157], v161 offset:22528
	s_waitcnt lgkmcnt(7)
	v_mfma_f32_16x16x32_f16 v[18:21], v[110:113], v[126:129], v[18:21]
	v_mfma_f32_16x16x32_f16 v[2:5], v[114:117], v[126:129], v[2:5]
	ds_read_b128 v[126:129], v161 offset:24576
	s_waitcnt lgkmcnt(7)
	v_mfma_f32_16x16x32_f16 v[26:29], v[110:113], v[130:133], v[26:29]
	v_mfma_f32_16x16x32_f16 v[10:13], v[114:117], v[130:133], v[10:13]
	ds_read_b128 v[130:133], v161 offset:26624
	s_waitcnt lgkmcnt(7)
	v_mfma_f32_16x16x32_f16 v[22:25], v[110:113], v[134:137], v[22:25]
	v_mfma_f32_16x16x32_f16 v[6:9], v[114:117], v[134:137], v[6:9]
	ds_read_b128 v[134:137], v161 offset:28672
	s_waitcnt lgkmcnt(7)
	v_mfma_f32_16x16x32_f16 v[30:33], v[110:113], v[138:141], v[30:33]
	v_mfma_f32_16x16x32_f16 v[14:17], v[114:117], v[138:141], v[14:17]
	ds_read_b128 v[138:141], v161 offset:30720
	s_waitcnt lgkmcnt(7)
	v_mfma_f32_16x16x32_f16 v[164:167], v[118:121], v[142:145], v[164:167]
	v_mfma_f32_16x16x32_f16 v[62:65], v[122:125], v[142:145], v[62:65]
	ds_read_b128 v[142:145], v161 offset:32768
	s_waitcnt lgkmcnt(7)
	v_mfma_f32_16x16x32_f16 v[86:89], v[118:121], v[146:149], v[86:89]
	v_mfma_f32_16x16x32_f16 v[58:61], v[122:125], v[146:149], v[58:61]
	ds_read_b128 v[146:149], v161 offset:34816
	s_waitcnt lgkmcnt(7)
	v_mfma_f32_16x16x32_f16 v[96:99], v[118:121], v[150:153], v[96:99]
	v_mfma_f32_16x16x32_f16 v[54:57], v[122:125], v[150:153], v[54:57]
	ds_read_b128 v[150:153], v161 offset:36864
	s_waitcnt lgkmcnt(7)
	v_mfma_f32_16x16x32_f16 v[82:85], v[118:121], v[154:157], v[82:85]
	v_mfma_f32_16x16x32_f16 v[50:53], v[122:125], v[154:157], v[50:53]
	ds_read_b128 v[154:157], v161 offset:38912
	s_waitcnt lgkmcnt(0)
	s_barrier
	s_mov_b32 m0, s28
	s_nop 0
	global_load_lds_dwordx4 v104, s[38:39]
	s_mov_b32 m0, s29
	s_nop 0
	global_load_lds_dwordx4 v105, s[38:39]
	s_mov_b32 m0, s30
	s_nop 0
	global_load_lds_dwordx4 v106, s[38:39]
	s_mov_b32 m0, s31
	s_nop 0
	global_load_lds_dwordx4 v107, s[38:39]
	s_mov_b32 m0, s32
	s_nop 0
	global_load_lds_dwordx4 v108, s[38:39]
	s_mov_b32 m0, s33
	s_nop 0
	global_load_lds_dwordx4 v109, s[38:39]
	s_add_u32 s38, s38, 0x80
	s_addc_u32 s39, s39, 0
	s_waitcnt lgkmcnt(7)
	v_mfma_f32_16x16x32_f16 v[78:81], v[118:121], v[126:129], v[78:81]
	v_mfma_f32_16x16x32_f16 v[46:49], v[122:125], v[126:129], v[46:49]
	s_waitcnt lgkmcnt(6)
	v_mfma_f32_16x16x32_f16 v[74:77], v[118:121], v[130:133], v[74:77]
	v_mfma_f32_16x16x32_f16 v[42:45], v[122:125], v[130:133], v[42:45]
	s_waitcnt lgkmcnt(5)
	v_mfma_f32_16x16x32_f16 v[70:73], v[118:121], v[134:137], v[70:73]
	v_mfma_f32_16x16x32_f16 v[38:41], v[122:125], v[134:137], v[38:41]
	s_waitcnt lgkmcnt(4)
	v_mfma_f32_16x16x32_f16 v[66:69], v[118:121], v[138:141], v[66:69]
	v_mfma_f32_16x16x32_f16 v[34:37], v[122:125], v[138:141], v[34:37]
	s_waitcnt lgkmcnt(3)
	v_mfma_f32_16x16x32_f16 v[18:21], v[118:121], v[142:145], v[18:21]
	v_mfma_f32_16x16x32_f16 v[2:5], v[122:125], v[142:145], v[2:5]
	s_waitcnt lgkmcnt(2)
	v_mfma_f32_16x16x32_f16 v[26:29], v[118:121], v[146:149], v[26:29]
	v_mfma_f32_16x16x32_f16 v[10:13], v[122:125], v[146:149], v[10:13]
	s_waitcnt lgkmcnt(1)
	v_mfma_f32_16x16x32_f16 v[22:25], v[118:121], v[150:153], v[22:25]
	v_mfma_f32_16x16x32_f16 v[6:9], v[122:125], v[150:153], v[6:9]
	s_waitcnt lgkmcnt(0)
	v_mfma_f32_16x16x32_f16 v[30:33], v[118:121], v[154:157], v[30:33]
	v_mfma_f32_16x16x32_f16 v[14:17], v[122:125], v[154:157], v[14:17]
	s_waitcnt vmcnt(0)
	s_barrier
	ds_read_b128 v[110:113], v158 offset:0
	ds_read_b128 v[114:117], v158 offset:2048
	ds_read_b128 v[118:121], v159 offset:0
	ds_read_b128 v[122:125], v159 offset:2048
	ds_read_b128 v[126:129], v160 offset:16384
	ds_read_b128 v[130:133], v160 offset:18432
	ds_read_b128 v[134:137], v160 offset:20480
	ds_read_b128 v[138:141], v160 offset:22528
	ds_read_b128 v[142:145], v160 offset:24576
	ds_read_b128 v[146:149], v160 offset:26624
	ds_read_b128 v[150:153], v160 offset:28672
	ds_read_b128 v[154:157], v160 offset:30720
	s_waitcnt lgkmcnt(7)
	v_mfma_f32_16x16x32_f16 v[164:167], v[110:113], v[126:129], v[164:167]
	v_mfma_f32_16x16x32_f16 v[62:65], v[114:117], v[126:129], v[62:65]
	ds_read_b128 v[126:129], v160 offset:32768
	s_waitcnt lgkmcnt(7)
	v_mfma_f32_16x16x32_f16 v[86:89], v[110:113], v[130:133], v[86:89]
	v_mfma_f32_16x16x32_f16 v[58:61], v[114:117], v[130:133], v[58:61]
	ds_read_b128 v[130:133], v160 offset:34816
	s_waitcnt lgkmcnt(10)
	s_barrier
	s_mov_b32 m0, s24
	s_nop 0
	global_load_lds_dwordx4 v100, s[36:37]
	s_mov_b32 m0, s25
	s_nop 0
	global_load_lds_dwordx4 v101, s[36:37]
	s_mov_b32 m0, s26
	s_nop 0
	global_load_lds_dwordx4 v102, s[36:37]
	s_mov_b32 m0, s27
	s_nop 0
	global_load_lds_dwordx4 v103, s[36:37]
	s_add_u32 s36, s36, 0x80
	s_addc_u32 s37, s37, 0
	s_waitcnt lgkmcnt(7)
	v_mfma_f32_16x16x32_f16 v[96:99], v[110:113], v[134:137], v[96:99]
	v_mfma_f32_16x16x32_f16 v[54:57], v[114:117], v[134:137], v[54:57]
	ds_read_b128 v[134:137], v160 offset:36864
	s_waitcnt lgkmcnt(7)
	v_mfma_f32_16x16x32_f16 v[82:85], v[110:113], v[138:141], v[82:85]
	v_mfma_f32_16x16x32_f16 v[50:53], v[114:117], v[138:141], v[50:53]
	ds_read_b128 v[138:141], v160 offset:38912
	s_waitcnt lgkmcnt(7)
	v_mfma_f32_16x16x32_f16 v[78:81], v[110:113], v[142:145], v[78:81]
	v_mfma_f32_16x16x32_f16 v[46:49], v[114:117], v[142:145], v[46:49]
	ds_read_b128 v[142:145], v161 offset:16384
	s_waitcnt lgkmcnt(7)
	v_mfma_f32_16x16x32_f16 v[74:77], v[110:113], v[146:149], v[74:77]
	v_mfma_f32_16x16x32_f16 v[42:45], v[114:117], v[146:149], v[42:45]
	ds_read_b128 v[146:149], v161 offset:18432
	s_waitcnt lgkmcnt(7)
	v_mfma_f32_16x16x32_f16 v[70:73], v[110:113], v[150:153], v[70:73]
	v_mfma_f32_16x16x32_f16 v[38:41], v[114:117], v[150:153], v[38:41]
	ds_read_b128 v[150:153], v161 offset:20480
	s_waitcnt lgkmcnt(7)
	v_mfma_f32_16x16x32_f16 v[66:69], v[110:113], v[154:157], v[66:69]
	v_mfma_f32_16x16x32_f16 v[34:37], v[114:117], v[154:157], v[34:37]
	ds_read_b128 v[154:157], v161 offset:22528
	s_waitcnt lgkmcnt(7)
	v_mfma_f32_16x16x32_f16 v[18:21], v[110:113], v[126:129], v[18:21]
	v_mfma_f32_16x16x32_f16 v[2:5], v[114:117], v[126:129], v[2:5]
	ds_read_b128 v[126:129], v161 offset:24576
	s_waitcnt lgkmcnt(7)
	v_mfma_f32_16x16x32_f16 v[26:29], v[110:113], v[130:133], v[26:29]
	v_mfma_f32_16x16x32_f16 v[10:13], v[114:117], v[130:133], v[10:13]
	ds_read_b128 v[130:133], v161 offset:26624
	s_waitcnt lgkmcnt(7)
	v_mfma_f32_16x16x32_f16 v[22:25], v[110:113], v[134:137], v[22:25]
	v_mfma_f32_16x16x32_f16 v[6:9], v[114:117], v[134:137], v[6:9]
	ds_read_b128 v[134:137], v161 offset:28672
	s_waitcnt lgkmcnt(7)
	v_mfma_f32_16x16x32_f16 v[30:33], v[110:113], v[138:141], v[30:33]
	v_mfma_f32_16x16x32_f16 v[14:17], v[114:117], v[138:141], v[14:17]
	ds_read_b128 v[138:141], v161 offset:30720
	s_waitcnt lgkmcnt(7)
	v_mfma_f32_16x16x32_f16 v[164:167], v[118:121], v[142:145], v[164:167]
	v_mfma_f32_16x16x32_f16 v[62:65], v[122:125], v[142:145], v[62:65]
	ds_read_b128 v[142:145], v161 offset:32768
	s_waitcnt lgkmcnt(7)
	v_mfma_f32_16x16x32_f16 v[86:89], v[118:121], v[146:149], v[86:89]
	v_mfma_f32_16x16x32_f16 v[58:61], v[122:125], v[146:149], v[58:61]
	ds_read_b128 v[146:149], v161 offset:34816
	s_waitcnt lgkmcnt(7)
	v_mfma_f32_16x16x32_f16 v[96:99], v[118:121], v[150:153], v[96:99]
	v_mfma_f32_16x16x32_f16 v[54:57], v[122:125], v[150:153], v[54:57]
	ds_read_b128 v[150:153], v161 offset:36864
	s_waitcnt lgkmcnt(7)
	v_mfma_f32_16x16x32_f16 v[82:85], v[118:121], v[154:157], v[82:85]
	v_mfma_f32_16x16x32_f16 v[50:53], v[122:125], v[154:157], v[50:53]
	ds_read_b128 v[154:157], v161 offset:38912
	s_waitcnt lgkmcnt(0)
	s_barrier
	s_mov_b32 m0, s28
	s_nop 0
	global_load_lds_dwordx4 v104, s[38:39]
	s_mov_b32 m0, s29
	s_nop 0
	global_load_lds_dwordx4 v105, s[38:39]
	s_mov_b32 m0, s30
	s_nop 0
	global_load_lds_dwordx4 v106, s[38:39]
	s_mov_b32 m0, s31
	s_nop 0
	global_load_lds_dwordx4 v107, s[38:39]
	s_mov_b32 m0, s32
	s_nop 0
	global_load_lds_dwordx4 v108, s[38:39]
	s_mov_b32 m0, s33
	s_nop 0
	global_load_lds_dwordx4 v109, s[38:39]
	s_add_u32 s38, s38, 0x80
	s_addc_u32 s39, s39, 0
	s_waitcnt lgkmcnt(7)
	v_mfma_f32_16x16x32_f16 v[78:81], v[118:121], v[126:129], v[78:81]
	v_mfma_f32_16x16x32_f16 v[46:49], v[122:125], v[126:129], v[46:49]
	s_waitcnt lgkmcnt(6)
	v_mfma_f32_16x16x32_f16 v[74:77], v[118:121], v[130:133], v[74:77]
	v_mfma_f32_16x16x32_f16 v[42:45], v[122:125], v[130:133], v[42:45]
	s_waitcnt lgkmcnt(5)
	v_mfma_f32_16x16x32_f16 v[70:73], v[118:121], v[134:137], v[70:73]
	v_mfma_f32_16x16x32_f16 v[38:41], v[122:125], v[134:137], v[38:41]
	s_waitcnt lgkmcnt(4)
	v_mfma_f32_16x16x32_f16 v[66:69], v[118:121], v[138:141], v[66:69]
	v_mfma_f32_16x16x32_f16 v[34:37], v[122:125], v[138:141], v[34:37]
	s_waitcnt lgkmcnt(3)
	v_mfma_f32_16x16x32_f16 v[18:21], v[118:121], v[142:145], v[18:21]
	v_mfma_f32_16x16x32_f16 v[2:5], v[122:125], v[142:145], v[2:5]
	s_waitcnt lgkmcnt(2)
	v_mfma_f32_16x16x32_f16 v[26:29], v[118:121], v[146:149], v[26:29]
	v_mfma_f32_16x16x32_f16 v[10:13], v[122:125], v[146:149], v[10:13]
	s_waitcnt lgkmcnt(1)
	v_mfma_f32_16x16x32_f16 v[22:25], v[118:121], v[150:153], v[22:25]
	v_mfma_f32_16x16x32_f16 v[6:9], v[122:125], v[150:153], v[6:9]
	s_waitcnt lgkmcnt(0)
	v_mfma_f32_16x16x32_f16 v[30:33], v[118:121], v[154:157], v[30:33]
	v_mfma_f32_16x16x32_f16 v[14:17], v[122:125], v[154:157], v[14:17]
	s_waitcnt vmcnt(0)
	s_barrier
	ds_read_b128 v[110:113], v158 offset:0
	ds_read_b128 v[114:117], v158 offset:2048
	ds_read_b128 v[118:121], v159 offset:0
	ds_read_b128 v[122:125], v159 offset:2048
	ds_read_b128 v[126:129], v160 offset:16384
	ds_read_b128 v[130:133], v160 offset:18432
	ds_read_b128 v[134:137], v160 offset:20480
	ds_read_b128 v[138:141], v160 offset:22528
	ds_read_b128 v[142:145], v160 offset:24576
	ds_read_b128 v[146:149], v160 offset:26624
	ds_read_b128 v[150:153], v160 offset:28672
	ds_read_b128 v[154:157], v160 offset:30720
	s_waitcnt lgkmcnt(7)
	v_mfma_f32_16x16x32_f16 v[164:167], v[110:113], v[126:129], v[164:167]
	v_mfma_f32_16x16x32_f16 v[62:65], v[114:117], v[126:129], v[62:65]
	ds_read_b128 v[126:129], v160 offset:32768
	s_waitcnt lgkmcnt(7)
	v_mfma_f32_16x16x32_f16 v[86:89], v[110:113], v[130:133], v[86:89]
	v_mfma_f32_16x16x32_f16 v[58:61], v[114:117], v[130:133], v[58:61]
	ds_read_b128 v[130:133], v160 offset:34816
	s_waitcnt lgkmcnt(7)
	v_mfma_f32_16x16x32_f16 v[96:99], v[110:113], v[134:137], v[96:99]
	v_mfma_f32_16x16x32_f16 v[54:57], v[114:117], v[134:137], v[54:57]
	ds_read_b128 v[134:137], v160 offset:36864
	s_waitcnt lgkmcnt(7)
	v_mfma_f32_16x16x32_f16 v[82:85], v[110:113], v[138:141], v[82:85]
	v_mfma_f32_16x16x32_f16 v[50:53], v[114:117], v[138:141], v[50:53]
	ds_read_b128 v[138:141], v160 offset:38912
	s_waitcnt lgkmcnt(7)
	v_mfma_f32_16x16x32_f16 v[78:81], v[110:113], v[142:145], v[78:81]
	v_mfma_f32_16x16x32_f16 v[46:49], v[114:117], v[142:145], v[46:49]
	ds_read_b128 v[142:145], v161 offset:16384
	s_waitcnt lgkmcnt(7)
	v_mfma_f32_16x16x32_f16 v[74:77], v[110:113], v[146:149], v[74:77]
	v_mfma_f32_16x16x32_f16 v[42:45], v[114:117], v[146:149], v[42:45]
	ds_read_b128 v[146:149], v161 offset:18432
	s_waitcnt lgkmcnt(7)
	v_mfma_f32_16x16x32_f16 v[70:73], v[110:113], v[150:153], v[70:73]
	v_mfma_f32_16x16x32_f16 v[38:41], v[114:117], v[150:153], v[38:41]
	ds_read_b128 v[150:153], v161 offset:20480
	s_waitcnt lgkmcnt(7)
	v_mfma_f32_16x16x32_f16 v[66:69], v[110:113], v[154:157], v[66:69]
	v_mfma_f32_16x16x32_f16 v[34:37], v[114:117], v[154:157], v[34:37]
	ds_read_b128 v[154:157], v161 offset:22528
	s_waitcnt lgkmcnt(7)
	v_mfma_f32_16x16x32_f16 v[18:21], v[110:113], v[126:129], v[18:21]
	v_mfma_f32_16x16x32_f16 v[2:5], v[114:117], v[126:129], v[2:5]
	ds_read_b128 v[126:129], v161 offset:24576
	s_waitcnt lgkmcnt(7)
	v_mfma_f32_16x16x32_f16 v[26:29], v[110:113], v[130:133], v[26:29]
	v_mfma_f32_16x16x32_f16 v[10:13], v[114:117], v[130:133], v[10:13]
	ds_read_b128 v[130:133], v161 offset:26624
	s_waitcnt lgkmcnt(7)
	v_mfma_f32_16x16x32_f16 v[22:25], v[110:113], v[134:137], v[22:25]
	v_mfma_f32_16x16x32_f16 v[6:9], v[114:117], v[134:137], v[6:9]
	ds_read_b128 v[134:137], v161 offset:28672
	s_waitcnt lgkmcnt(7)
	v_mfma_f32_16x16x32_f16 v[30:33], v[110:113], v[138:141], v[30:33]
	v_mfma_f32_16x16x32_f16 v[14:17], v[114:117], v[138:141], v[14:17]
	ds_read_b128 v[138:141], v161 offset:30720
	s_waitcnt lgkmcnt(7)
	v_mfma_f32_16x16x32_f16 v[164:167], v[118:121], v[142:145], v[164:167]
	v_mfma_f32_16x16x32_f16 v[62:65], v[122:125], v[142:145], v[62:65]
	ds_read_b128 v[142:145], v161 offset:32768
	s_waitcnt lgkmcnt(7)
	v_mfma_f32_16x16x32_f16 v[86:89], v[118:121], v[146:149], v[86:89]
	v_mfma_f32_16x16x32_f16 v[58:61], v[122:125], v[146:149], v[58:61]
	ds_read_b128 v[146:149], v161 offset:34816
	s_waitcnt lgkmcnt(7)
	v_mfma_f32_16x16x32_f16 v[96:99], v[118:121], v[150:153], v[96:99]
	v_mfma_f32_16x16x32_f16 v[54:57], v[122:125], v[150:153], v[54:57]
	ds_read_b128 v[150:153], v161 offset:36864
	s_waitcnt lgkmcnt(7)
	v_mfma_f32_16x16x32_f16 v[82:85], v[118:121], v[154:157], v[82:85]
	v_mfma_f32_16x16x32_f16 v[50:53], v[122:125], v[154:157], v[50:53]
	ds_read_b128 v[154:157], v161 offset:38912
	s_waitcnt lgkmcnt(0)
	s_barrier
	s_waitcnt lgkmcnt(7)
	v_mfma_f32_16x16x32_f16 v[78:81], v[118:121], v[126:129], v[78:81]
	v_mfma_f32_16x16x32_f16 v[46:49], v[122:125], v[126:129], v[46:49]
	s_waitcnt lgkmcnt(6)
	v_mfma_f32_16x16x32_f16 v[74:77], v[118:121], v[130:133], v[74:77]
	v_mfma_f32_16x16x32_f16 v[42:45], v[122:125], v[130:133], v[42:45]
	s_waitcnt lgkmcnt(5)
	v_mfma_f32_16x16x32_f16 v[70:73], v[118:121], v[134:137], v[70:73]
	v_mfma_f32_16x16x32_f16 v[38:41], v[122:125], v[134:137], v[38:41]
	s_waitcnt lgkmcnt(4)
	v_mfma_f32_16x16x32_f16 v[66:69], v[118:121], v[138:141], v[66:69]
	v_mfma_f32_16x16x32_f16 v[34:37], v[122:125], v[138:141], v[34:37]
	s_waitcnt lgkmcnt(3)
	v_mfma_f32_16x16x32_f16 v[18:21], v[118:121], v[142:145], v[18:21]
	v_mfma_f32_16x16x32_f16 v[2:5], v[122:125], v[142:145], v[2:5]
	s_waitcnt lgkmcnt(2)
	v_mfma_f32_16x16x32_f16 v[26:29], v[118:121], v[146:149], v[26:29]
	v_mfma_f32_16x16x32_f16 v[10:13], v[122:125], v[146:149], v[10:13]
	s_waitcnt lgkmcnt(1)
	v_mfma_f32_16x16x32_f16 v[22:25], v[118:121], v[150:153], v[22:25]
	v_mfma_f32_16x16x32_f16 v[6:9], v[122:125], v[150:153], v[6:9]
	s_waitcnt lgkmcnt(0)
	v_mfma_f32_16x16x32_f16 v[30:33], v[118:121], v[154:157], v[30:33]
	v_mfma_f32_16x16x32_f16 v[14:17], v[122:125], v[154:157], v[14:17]
	s_nop 15
	s_nop 15
	s_movk_i32 s2, 0xfc
	v_cmp_gt_u32_e32 vcc, s2, v0
	s_mov_b32 s2, 0x12492493
	s_movk_i32 s4, 0x380
	s_movk_i32 s12, 0x110
	v_cmp_gt_u32_e64 s[4:5], s4, v0
	s_setprio 2
	v_lshrrev_b32_e32 v93, 1, v0
	v_cndmask_b32_e32 v94, 0, v93, vcc
	s_nop 5
	v_cvt_f16_f32_e32 v86, v86
	s_nop 5
	v_cvt_f16_f32_e32 v54, v54
	v_cvt_f16_f32_e32 v82, v82
	v_cvt_f16_f32_e32 v50, v50
	s_nop 5
	v_cvt_f16_f32_e32 v78, v78
	v_mul_i32_i24_e32 v102, 0xffffffc2, v92
	v_mul_u32_u24_e32 v101, 0x110, v91
	v_lshlrev_b32_e32 v91, 6, v92
	v_add3_u32 v91, v91, v102, v101
	ds_write_b16 v91, v86 offset:32
	v_cvt_f16_f32_e32 v86, v87
	v_cvt_f16_f32_e32 v74, v74
	v_cvt_f16_f32_e32 v102, v165
	ds_write_b16 v91, v86 offset:304
	v_cvt_f16_f32_e32 v86, v88
	s_nop 2
	v_cvt_f16_f32_e32 v34, v34
	ds_write_b16 v91, v82 offset:96
	ds_write_b16 v91, v86 offset:576
	v_cvt_f16_f32_e32 v86, v89
	v_cvt_f16_f32_e32 v38, v38
	ds_write_b16 v91, v34 offset:4576
	ds_write_b16 v91, v86 offset:848
	v_cvt_f16_f32_e32 v86, v96
	s_nop 1
	v_cvt_f16_f32_e32 v62, v62
	v_cvt_f16_f32_e32 v34, v35
	s_nop 0
	v_cvt_f16_f32_e32 v58, v58
	ds_write_b16 v91, v38 offset:4544
	v_cvt_f16_f32_e32 v38, v39
	s_nop 1
	v_cvt_f16_f32_e32 v46, v46
	ds_write_b16 v91, v86 offset:64
	v_cvt_f16_f32_e32 v86, v97
	s_nop 0
	v_cvt_f16_f32_e32 v42, v42
	v_cvt_f16_f32_e32 v82, v83
	ds_write_b16 v91, v78 offset:128
	s_nop 1
	v_cvt_f16_f32_e32 v70, v70
	v_cvt_f16_f32_e32 v78, v79
	ds_write_b16 v91, v74 offset:160
	v_cvt_f16_f32_e32 v74, v75
	s_nop 0
	v_cvt_f16_f32_e32 v66, v66
	ds_write_b16 v91, v70 offset:192
	v_cvt_f16_f32_e32 v70, v71
	ds_write_b16 v91, v62 offset:4352
	ds_write_b16 v91, v66 offset:224
	v_cvt_f16_f32_e32 v66, v67
	v_cvt_f16_f32_e32 v62, v63
	ds_write_b16 v91, v58 offset:4384
	v_cvt_f16_f32_e32 v58, v59
	ds_write_b16 v91, v54 offset:4416
	v_cvt_f16_f32_e32 v54, v55
	ds_write_b16 v91, v50 offset:4448
	v_cvt_f16_f32_e32 v50, v51
	ds_write_b16 v91, v46 offset:4480
	v_cvt_f16_f32_e32 v46, v47
	ds_write_b16 v91, v42 offset:4512
	v_cvt_f16_f32_e32 v42, v43
	ds_write_b16 v91, v34 offset:4848
	v_cvt_f16_f32_e32 v34, v36
	ds_write_b16 v91, v38 offset:4816
	v_cvt_f16_f32_e32 v38, v40
	ds_write_b16 v91, v102 offset:272
	v_cvt_f16_f32_e32 v102, v166
	ds_write_b16 v91, v86 offset:336
	v_cvt_f16_f32_e32 v86, v98
	ds_write_b16 v91, v82 offset:368
	v_cvt_f16_f32_e32 v82, v84
	ds_write_b16 v91, v78 offset:400
	v_cvt_f16_f32_e32 v78, v80
	ds_write_b16 v91, v74 offset:432
	v_cvt_f16_f32_e32 v74, v76
	ds_write_b16 v91, v70 offset:464
	v_cvt_f16_f32_e32 v70, v72
	ds_write_b16 v91, v66 offset:496
	v_cvt_f16_f32_e32 v66, v68
	ds_write_b16 v91, v62 offset:4624
	v_cvt_f16_f32_e32 v62, v64
	ds_write_b16 v91, v58 offset:4656
	v_cvt_f16_f32_e32 v58, v60
	ds_write_b16 v91, v54 offset:4688
	v_cvt_f16_f32_e32 v54, v56
	ds_write_b16 v91, v50 offset:4720
	v_cvt_f16_f32_e32 v50, v52
	ds_write_b16 v91, v46 offset:4752
	v_cvt_f16_f32_e32 v46, v48
	ds_write_b16 v91, v42 offset:4784
	v_cvt_f16_f32_e32 v42, v44
	ds_write_b16 v91, v34 offset:5120
	v_cvt_f16_f32_e32 v34, v37
	ds_write_b16 v91, v38 offset:5088
	v_cvt_f16_f32_e32 v38, v41
	v_cvt_f16_f32_e32 v103, v164
	ds_write_b16 v91, v102 offset:544
	v_cvt_f16_f32_e32 v102, v167
	ds_write_b16 v91, v86 offset:608
	v_cvt_f16_f32_e32 v86, v99
	ds_write_b16 v91, v82 offset:640
	v_cvt_f16_f32_e32 v82, v85
	ds_write_b16 v91, v78 offset:672
	v_cvt_f16_f32_e32 v78, v81
	ds_write_b16 v91, v74 offset:704
	v_cvt_f16_f32_e32 v74, v77
	ds_write_b16 v91, v70 offset:736
	v_cvt_f16_f32_e32 v70, v73
	ds_write_b16 v91, v66 offset:768
	v_cvt_f16_f32_e32 v66, v69
	ds_write_b16 v91, v62 offset:4896
	v_cvt_f16_f32_e32 v62, v65
	ds_write_b16 v91, v58 offset:4928
	v_cvt_f16_f32_e32 v58, v61
	ds_write_b16 v91, v54 offset:4960
	v_cvt_f16_f32_e32 v54, v57
	ds_write_b16 v91, v50 offset:4992
	v_cvt_f16_f32_e32 v50, v53
	ds_write_b16 v91, v46 offset:5024
	v_cvt_f16_f32_e32 v46, v49
	ds_write_b16 v91, v42 offset:5056
	v_cvt_f16_f32_e32 v42, v45
	ds_write_b16 v91, v34 offset:5392
	v_min_u32_e32 v34, 8, v92
	v_mul_hi_u32 v100, v94, s2
	ds_write_b16 v91, v38 offset:5360
	v_cmp_gt_u32_e64 s[2:3], 9, v92
	v_mul_u32_u24_e32 v39, 14, v34
	v_and_b32_e32 v40, 48, v0
	v_lshlrev_b32_e32 v38, 2, v92
	ds_write_b16 v91, v103
	ds_write_b16 v91, v102 offset:816
	ds_write_b16 v91, v86 offset:880
	ds_write_b16 v91, v82 offset:912
	ds_write_b16 v91, v78 offset:944
	ds_write_b16 v91, v74 offset:976
	ds_write_b16 v91, v70 offset:1008
	ds_write_b16 v91, v66 offset:1040
	ds_write_b16 v91, v62 offset:5168
	ds_write_b16 v91, v58 offset:5200
	ds_write_b16 v91, v54 offset:5232
	ds_write_b16 v91, v50 offset:5264
	ds_write_b16 v91, v46 offset:5296
	ds_write_b16 v91, v42 offset:5328
	s_waitcnt lgkmcnt(0)
	s_barrier
	s_and_saveexec_b64 s[6:7], s[4:5]
	s_cbranch_execz .LBB1_9
	v_add_u32_e32 v34, v1, v39
	v_mad_u32_u24 v41, v34, s12, v40
	ds_read_b128 v[34:37], v41
	ds_read_b128 v[42:45], v41 offset:64
	ds_read_b128 v[46:49], v41 offset:128
	ds_read_b128 v[50:53], v41 offset:192
	v_cmp_ne_u32_e64 s[4:5], 3, v90
	v_mul_u32_u24_e32 v41, 9, v1
	s_and_b64 s[12:13], s[4:5], s[2:3]
	s_waitcnt lgkmcnt(1)
	v_mfma_f32_16x16x32_f16 v[34:37], v[34:37], v[46:49], 0
	s_waitcnt lgkmcnt(0)
	v_mfma_f32_16x16x32_f16 v[34:37], v[42:45], v[50:53], v[34:37]
	s_and_saveexec_b64 s[4:5], s[12:13]
	v_add_u32_e32 v42, v95, v41
	s_nop 5
	v_mul_f32_e32 v34, 0x3e000000, v34
	v_mad_u32_u24 v42, v42, 48, v38
	ds_write_b32 v42, v34 offset:35328
	s_or_b64 exec, exec, s[4:5]
	v_or_b32_e32 v34, 1, v95
	v_cmp_gt_u32_e64 s[4:5], 9, v34
	s_and_b64 s[12:13], s[4:5], s[2:3]
	s_and_saveexec_b64 s[4:5], s[12:13]
	v_add_u32_e32 v34, v34, v41
	v_mul_f32_e32 v35, 0x3e000000, v35
	v_mad_u32_u24 v34, v34, 48, v38
	ds_write_b32 v34, v35 offset:35328
	s_or_b64 exec, exec, s[4:5]
	v_or_b32_e32 v34, 2, v95
	v_cmp_gt_u32_e64 s[4:5], 9, v34
	s_and_b64 s[12:13], s[4:5], s[2:3]
	s_and_saveexec_b64 s[4:5], s[12:13]
	v_add_u32_e32 v34, v34, v41
	v_mul_f32_e32 v35, 0x3e000000, v36
	v_mad_u32_u24 v34, v34, 48, v38
	ds_write_b32 v34, v35 offset:35328
	s_or_b64 exec, exec, s[4:5]
	v_or_b32_e32 v34, 3, v95
	v_cmp_gt_u32_e64 s[4:5], 9, v34
	s_and_b64 s[4:5], s[4:5], s[2:3]
	s_and_b64 exec, exec, s[4:5]
	v_add_u32_e32 v34, v34, v41
	v_mul_f32_e32 v35, 0x3e000000, v37
	v_mad_u32_u24 v34, v34, 48, v38
	ds_write_b32 v34, v35 offset:35328
